# final combine/LN2 phase: loop-top full vmcnt drain replaced by vmcnt(8) so the 8 output stores of a row retire under the next row's loads
# speedup vs baseline: 1.0024x; 1.0004x over previous
; #define LAS __attribute__((address_space(3)))
; __device__ __forceinline__ void phase9(Frame& F, const Args& a) {
;     ...
;     LAS float* prm = (LAS float*)(F.lds);
;     for (int i = F.tid; i < D / 4; i += NWAVES * 64) { ((LAS f32x4*)prm)[i] = ((const f32x4*)a.ln2_g)[i]; ((LAS f32x4*)(prm + D))[i] = ((const f32x4*)a.ln2_b)[i];
; #pragma unroll
;         for (int b = 0; b < BATCH; ++b) ((LAS f32x4*)(prm + (2 + b) * D))[i] = ((const f32x4*)(mod + (size_t)b * (6 * D) + 5 * D))[i]; }
;     __syncthreads();
;     int sln[4] = {0, 0, 0, 0}; float gtn[4] = {0.f, 0.f, 0.f, 0.f};
;     if (gw < T) {
; #pragma unroll
;         for (int k = 0; k < 4; ++k) { sln[k] = TSLOT[gw * 4 + k]; gtn[k] = GATE[gw * 4 + k]; } }
;     ...
;         for (int j = 0; j < 8; ++j) { const f32x4 gg = *((const LAS f32x4*)prm + F.lane + 64 * j), bb = *((const LAS f32x4*)(prm + D) + F.lane + 64 * j);
.LBB0_940:
	s_or_b64 exec, exec, s[0:1]
	s_lshl_b32 s0, s48, 3
	s_add_i32 s0, s0, s49
	s_cmpk_gt_i32 s0, 0x3fff
	s_waitcnt lgkmcnt(0)
	s_barrier
	s_cbranch_scc1 .LBB0_945
	s_lshl_b32 s2, s33, 3
	s_add_u32 s11, s76, 0xac0000
	s_addc_u32 s14, s77, 0
	s_add_u32 s15, s76, 0xa40000
	s_addc_u32 s16, s77, 0
	s_lshl_b32 s4, s0, 2
	s_ashr_i32 s5, s4, 31
	s_lshl_b64 s[4:5], s[4:5], 2
	s_add_u32 s6, s11, s4
	s_addc_u32 s7, s14, s5
	s_waitcnt vmcnt(14)
	v_mov_b32_e32 v73, 0
	s_add_u32 s4, s15, s4
	s_addc_u32 s5, s16, s5
	global_load_dwordx4 v[68:71], v73, s[6:7]
	global_load_dwordx4 v[64:67], v73, s[4:5]
	s_waitcnt vmcnt(15)
	v_and_b32_e32 v76, 63, v0
	v_lshlrev_b32_e32 v72, 2, v76
	s_waitcnt vmcnt(14)
	v_lshlrev_b32_e32 v78, 4, v76
	v_lshl_add_u64 v[0:1], s[76:77], 0, v[72:73]
	s_mov_b64 s[4:5], 0x49000000
	s_waitcnt vmcnt(5)
	v_add_u32_e32 v116, 0, v78
	v_lshl_add_u64 v[74:75], v[0:1], 0, s[4:5]
	s_waitcnt vmcnt(2)
	ds_read_b128 v[0:3], v116
	ds_read_b128 v[4:7], v116 offset:1024
	ds_read_b128 v[8:11], v116 offset:8192
	ds_read_b128 v[12:15], v116 offset:9216
	ds_read_b128 v[16:19], v116 offset:2048
	ds_read_b128 v[20:23], v116 offset:3072
	ds_read_b128 v[24:27], v116 offset:10240
	ds_read_b128 v[28:31], v116 offset:11264
	ds_read_b128 v[32:35], v116 offset:4096
	ds_read_b128 v[36:39], v116 offset:5120
	ds_read_b128 v[40:43], v116 offset:12288
	ds_read_b128 v[44:47], v116 offset:13312
	ds_read_b128 v[48:51], v116 offset:6144
	ds_read_b128 v[52:55], v116 offset:7168
	ds_read_b128 v[56:59], v116 offset:14336
	ds_read_b128 v[60:63], v116 offset:15360
	s_add_i32 s1, s0, s2
	s_lshl_b32 s1, s1, 2
	s_or_b32 s4, s1, 3
	s_ashr_i32 s1, s0, 31
	s_lshl_b32 s17, s33, 5
	s_lshl_b64 s[6:7], s[0:1], 12
	s_add_u32 s6, s76, s6
	v_lshlrev_b32_e32 v72, 3, v76
	s_addc_u32 s7, s77, s7
	v_lshl_add_u64 v[76:77], s[6:7], 0, v[72:73]
	s_mov_b64 s[6:7], 0x24000000
	s_ashr_i32 s3, s2, 31
	v_lshl_add_u64 v[76:77], v[76:77], 0, s[6:7]
	s_lshl_b64 s[6:7], s[2:3], 12
	s_lshl_b64 s[8:9], s[0:1], 13
	s_add_u32 s8, s74, s8
	v_mov_b32_e32 v79, v73
	s_addc_u32 s9, s75, s9
	v_lshl_add_u64 v[78:79], s[8:9], 0, v[78:79]
	s_mov_b64 s[8:9], 0x1000
	v_lshl_add_u64 v[78:79], v[78:79], 0, s[8:9]
	s_lshl_b64 s[8:9], s[2:3], 13
	s_mov_b32 s10, 0x3f9837f0
	v_mov_b32_e32 v72, 0x3727c5ac
	s_mov_b32 s3, 0xf800000
	v_mov_b32_e32 v117, 0x260
	s_waitcnt vmcnt(0)
	s_branch .LBB0_943

; #define LAS __attribute__((address_space(3)))
; __device__ __forceinline__ void phase9(Frame& F, const Args& a) {
;     ...
;     for (int m = gw; m < T; m += NGW) {
;         f32x4* xo = (f32x4*)(a.out + (size_t)m * D) + F.lane; const v2u* xi = (const v2u*)(X1 + (size_t)m * D) + F.lane;
;         const LAS float* mb = prm + (2 + m / SEQ) * D;
;         int sl[4]; float gt[4];
; #pragma unroll
;         for (int k = 0; k < 4; ++k) { sl[k] = sln[k]; gt[k] = gtn[k] * (1.0f / SC_YS); }
;         if (m + NGW < T) {
; #pragma unroll
;             for (int k = 0; k < 4; ++k) { sln[k] = TSLOT[(m + NGW) * 4 + k]; gtn[k] = GATE[(m + NGW) * 4 + k]; } }
.LBB0_943:
	s_add_i32 s18, s0, s2
	s_cmpk_gt_i32 s18, 0x3fff
	s_cselect_b64 s[12:13], -1, 0
	s_and_b64 vcc, exec, s[12:13]
	s_waitcnt vmcnt(8)
	v_mov_b64_e32 v[86:87], v[66:67]
	v_mov_b64_e32 v[82:83], v[64:65]
	v_mov_b64_e32 v[84:85], v[70:71]
	v_mov_b64_e32 v[80:81], v[68:69]
	s_cbranch_vccnz .LBB0_942
	s_add_i32 s20, s4, -3
	s_ashr_i32 s21, s20, 31
	s_lshl_b64 s[20:21], s[20:21], 2
	s_add_u32 s22, s11, s20
	s_addc_u32 s23, s14, s21
	s_add_u32 s20, s15, s20
	s_addc_u32 s21, s16, s21
	s_add_i32 s24, s4, -2
	s_ashr_i32 s25, s24, 31
	s_lshl_b64 s[24:25], s[24:25], 2
	s_add_u32 s26, s11, s24
	s_addc_u32 s27, s14, s25
	s_add_u32 s24, s15, s24
	s_addc_u32 s25, s16, s25
	s_add_i32 s28, s4, -1
	s_ashr_i32 s29, s28, 31
	s_lshl_b64 s[28:29], s[28:29], 2
	s_add_u32 s30, s11, s28
	s_addc_u32 s31, s14, s29
	s_add_u32 s28, s15, s28
	s_addc_u32 s29, s16, s29
	s_ashr_i32 s5, s4, 31
	s_lshl_b64 s[34:35], s[4:5], 2
	s_add_u32 s36, s11, s34
	s_addc_u32 s37, s14, s35
	s_add_u32 s34, s15, s34
	s_addc_u32 s35, s16, s35
	global_load_dword v80, v73, s[22:23]
	global_load_dword v82, v73, s[20:21]
	global_load_dword v81, v73, s[26:27]
	global_load_dword v83, v73, s[24:25]
	global_load_dword v84, v73, s[30:31]
	global_load_dword v86, v73, s[28:29]
	global_load_dword v85, v73, s[36:37]
	global_load_dword v87, v73, s[34:35]
	s_branch .LBB0_942
